# dilated attention: q-fragment loads of an item requested at the item top (overlapping the K/V LDS fill) instead of right before vmcnt(0)+barrier; fill waits counted vmcnt(4)
# speedup vs baseline: 1.0312x; 1.0047x over previous
.LBB0_235:
	s_ashr_i32 s0, s33, 5
	s_mul_hi_i32 s1, s0, 0x55555556
	s_lshr_b32 s14, s1, 31
	s_add_i32 s1, s1, s14
	s_mul_i32 s1, s1, 3
	s_sub_i32 s14, s0, s1
	s_cmp_eq_u32 s14, 1
	s_cselect_b64 s[16:17], -1, 0
	s_and_b64 s[0:1], s[16:17], exec
	s_cselect_b32 s15, 2, 4
	s_cmp_eq_u32 s14, 0
	s_cselect_b64 s[18:19], -1, 0
	s_and_b64 s[0:1], s[18:19], exec
	s_cselect_b32 s34, 0, s15
	s_and_b32 s0, s30, 0x1f00
	s_sub_i32 s1, 13, s34
	s_lshr_b32 s35, s0, s1
	s_lshl_b32 s1, s35, s1
	s_sub_i32 s15, s0, s1
	s_mul_hi_i32 s42, s33, 0x2aaaaaab
	s_lshr_b32 s43, s42, 31
	s_ashr_i32 s42, s42, 4
	s_add_i32 s42, s42, s43
	s_and_b32 s43, s42, 15
	s_lshl_b32 s48, s43, 7
	s_mov_b32 s49, 0
	s_lshl_b32 s42, s42, 9
	s_and_b32 s42, s42, 0xffffe000
	s_or_b32 s42, s35, s42
	s_add_i32 s44, s15, s3
	v_add_u32_e32 v214, s44, v160
	v_lshlrev_b32_e32 v215, s34, v214
	v_add_u32_e32 v215, s42, v215
	v_mov_b64_e32 v[212:213], s[12:13]
	s_movk_i32 s45, 0x4800
	v_mad_i64_i32 v[212:213], s[46:47], v215, s45, v[212:213]
	s_mul_i32 s46, s14, 0xc00
	s_ashr_i32 s47, s46, 31
	v_lshl_add_u64 v[212:213], s[46:47], 1, v[212:213]
	v_lshl_add_u64 v[212:213], v[212:213], 0, s[48:49]
	v_lshl_add_u64 v[212:213], v[212:213], 0, v[0:1]
	global_load_dwordx4 v[134:137], v[212:213], off
	global_load_dwordx4 v[130:133], v[212:213], off offset:32
	global_load_dwordx4 v[126:129], v[212:213], off offset:64
	global_load_dwordx4 v[122:125], v[212:213], off offset:96
	v_mov_b32_e32 v19, v155
	s_sub_i32 s31, 0x7f, s15
	v_lshlrev_b32_e32 v18, 3, v19
	v_ashrrev_i32_e32 v20, 3, v19
	v_and_b32_e32 v18, 56, v18
	v_cmp_lt_i32_e32 vcc, s31, v20
	s_and_saveexec_b64 s[0:1], vcc
	s_cbranch_execz .LBB0_237
	s_movk_i32 s25, 0x48
	v_mad_u64_u32 v[20:21], s[36:37], v20, s25, v[18:19]
	v_lshl_add_u32 v20, v20, 1, 0
	s_waitcnt vmcnt(4)
	ds_write_b128 v20, v[106:109]
.LBB0_237:
	s_or_b64 exec, exec, s[0:1]
	v_add_u32_e32 v20, 0x200, v19
	v_ashrrev_i32_e32 v21, 3, v20
	v_cmp_lt_i32_e32 vcc, s31, v21
	s_and_saveexec_b64 s[0:1], vcc
	s_cbranch_execz .LBB0_239
	s_movk_i32 s25, 0x48
	v_mad_u64_u32 v[22:23], s[36:37], v21, s25, v[18:19]
	v_lshl_add_u32 v21, v22, 1, 0
	s_waitcnt vmcnt(4)
	ds_write_b128 v21, v[98:101]
.LBB0_239:
	s_or_b64 exec, exec, s[0:1]
	v_add_u32_e32 v21, 0x400, v19
	v_ashrrev_i32_e32 v21, 3, v21
	v_cmp_lt_i32_e32 vcc, s31, v21
	s_and_saveexec_b64 s[0:1], vcc
	s_cbranch_execz .LBB0_241
	s_movk_i32 s25, 0x48
	v_mad_u64_u32 v[22:23], s[36:37], v21, s25, v[18:19]
	v_lshl_add_u32 v21, v22, 1, 0
	s_waitcnt vmcnt(4)
	ds_write_b128 v21, v[114:117]
.LBB0_241:
	s_or_b64 exec, exec, s[0:1]
	v_add_u32_e32 v21, 0x600, v19
	v_ashrrev_i32_e32 v21, 3, v21
	v_cmp_lt_i32_e32 vcc, s31, v21
	s_and_saveexec_b64 s[0:1], vcc
	s_cbranch_execz .LBB0_243
	s_movk_i32 s25, 0x48
	v_mad_u64_u32 v[22:23], s[36:37], v21, s25, v[18:19]
	v_lshl_add_u32 v21, v22, 1, 0
	s_waitcnt vmcnt(4)
	ds_write_b128 v21, v[102:105]
.LBB0_243:
	s_or_b64 exec, exec, s[0:1]
	v_add_u32_e32 v21, 0x800, v19
	v_ashrrev_i32_e32 v21, 3, v21
	v_cmp_lt_i32_e32 vcc, s31, v21
	s_and_saveexec_b64 s[0:1], vcc
	s_cbranch_execz .LBB0_245
	s_movk_i32 s25, 0x48
	v_mad_u64_u32 v[22:23], s[36:37], v21, s25, v[18:19]
	v_lshl_add_u32 v21, v22, 1, 0
	s_waitcnt vmcnt(4)
	ds_write_b128 v21, v[118:121]
.LBB0_245:
	s_or_b64 exec, exec, s[0:1]
	v_add_u32_e32 v21, 0xa00, v19
	v_ashrrev_i32_e32 v21, 3, v21
	v_cmp_lt_i32_e32 vcc, s31, v21
	s_and_saveexec_b64 s[0:1], vcc
	s_cbranch_execz .LBB0_247
	s_movk_i32 s25, 0x48
	v_mad_u64_u32 v[22:23], s[36:37], v21, s25, v[18:19]
	v_lshl_add_u32 v21, v22, 1, 0
	s_waitcnt vmcnt(4)
	ds_write_b128 v21, v[110:113]
.LBB0_247:
	s_or_b64 exec, exec, s[0:1]
	v_ashrrev_i32_e32 v21, 1, v19
	v_and_b32_e32 v24, -4, v21
	s_movk_i32 s0, 0x300
	v_cmp_gt_i32_e32 vcc, s0, v19
	v_cmp_lt_i32_e64 s[0:1], s31, v24
	s_and_b64 s[36:37], vcc, s[0:1]
	v_mov_b32_e32 v21, 0x308
	s_movk_i32 s0, 0x184
	v_mad_u32_u24 v23, v18, s0, v21
	v_mov_b32_e32 v21, 0x610
	v_mad_u32_u24 v22, v18, s0, v21
	v_mov_b32_e32 v21, 0x918
	v_mad_u32_u24 v21, v18, s0, v21
	s_and_saveexec_b64 s[0:1], s[36:37]
	s_cbranch_execz .LBB0_249
	s_movk_i32 s25, 0x184
	s_mov_b32 s36, 0x5040100
	v_mad_u32_u24 v30, v18, s25, v24
	v_add_u32_e32 v25, 0x184, v24
	s_waitcnt vmcnt(4)
	v_perm_b32 v26, v86, v82, s36
	v_perm_b32 v27, v94, v90, s36
	v_lshl_add_u32 v30, v30, 1, 0
	s_mov_b32 s37, 0x7060302
	ds_write_b64 v30, v[26:27] offset:55296
	v_mad_u32_u24 v26, v18, s25, v25
	v_perm_b32 v28, v86, v82, s37
	v_perm_b32 v29, v94, v90, s37
	v_lshl_add_u32 v26, v26, 1, 0
	v_add_u32_e32 v30, v23, v24
	ds_write_b64 v26, v[28:29] offset:55296
	v_perm_b32 v26, v87, v83, s36
	v_perm_b32 v27, v95, v91, s36
	v_lshl_add_u32 v30, v30, 1, 0
	ds_write_b64 v30, v[26:27] offset:55296
	v_add_u32_e32 v26, v23, v25
	v_perm_b32 v28, v87, v83, s37
	v_perm_b32 v29, v95, v91, s37
	v_lshl_add_u32 v26, v26, 1, 0
	v_add_u32_e32 v30, v22, v24
	ds_write_b64 v26, v[28:29] offset:55296
	v_perm_b32 v26, v88, v84, s36
	v_perm_b32 v27, v96, v92, s36
	v_lshl_add_u32 v30, v30, 1, 0
	ds_write_b64 v30, v[26:27] offset:55296
	v_add_u32_e32 v26, v22, v25
	v_perm_b32 v28, v88, v84, s37
	v_perm_b32 v29, v96, v92, s37
	v_lshl_add_u32 v26, v26, 1, 0
	v_add_u32_e32 v24, v21, v24
	ds_write_b64 v26, v[28:29] offset:55296
	v_perm_b32 v26, v89, v85, s36
	v_perm_b32 v27, v97, v93, s36
	v_lshl_add_u32 v24, v24, 1, 0
	ds_write_b64 v24, v[26:27] offset:55296
	v_add_u32_e32 v24, v21, v25
	v_perm_b32 v28, v89, v85, s37
	v_perm_b32 v29, v97, v93, s37
	v_lshl_add_u32 v24, v24, 1, 0
	ds_write_b64 v24, v[28:29] offset:55296
.LBB0_249:
	s_or_b64 exec, exec, s[0:1]
	v_ashrrev_i32_e32 v20, 1, v20
	v_and_b32_e32 v20, -4, v20
	s_movk_i32 s0, 0x100
	v_cmp_gt_i32_e32 vcc, s0, v19
	v_cmp_lt_i32_e64 s[0:1], s31, v20
	s_and_b64 s[36:37], vcc, s[0:1]
	s_and_saveexec_b64 s[0:1], s[36:37]
	s_cbranch_execz .LBB0_251
	v_add_u32_e32 v28, 0x184, v20
	s_movk_i32 s25, 0x184
	s_mov_b32 s31, 0x5040100
	s_mov_b32 s36, 0x7060302
	v_mad_u32_u24 v19, v18, s25, v20
	v_mad_u32_u24 v18, v18, s25, v28
	s_waitcnt vmcnt(4)
	v_perm_b32 v24, v70, v66, s31
	v_perm_b32 v25, v78, v74, s31
	v_perm_b32 v26, v70, v66, s36
	v_perm_b32 v27, v78, v74, s36
	v_lshl_add_u32 v19, v19, 1, 0
	v_lshl_add_u32 v18, v18, 1, 0
	ds_write_b64 v19, v[24:25] offset:55296
	ds_write_b64 v18, v[26:27] offset:55296
	v_add_u32_e32 v26, v23, v20
	v_perm_b32 v18, v71, v67, s31
	v_perm_b32 v19, v79, v75, s31
	v_lshl_add_u32 v26, v26, 1, 0
	ds_write_b64 v26, v[18:19] offset:55296
	v_add_u32_e32 v18, v28, v23
	v_perm_b32 v24, v71, v67, s36
	v_perm_b32 v25, v79, v75, s36
	v_lshl_add_u32 v18, v18, 1, 0
	v_add_u32_e32 v23, v22, v20
	ds_write_b64 v18, v[24:25] offset:55296
	v_perm_b32 v18, v72, v68, s31
	v_perm_b32 v19, v80, v76, s31
	v_lshl_add_u32 v23, v23, 1, 0
	ds_write_b64 v23, v[18:19] offset:55296
	v_add_u32_e32 v18, v28, v22
	v_perm_b32 v24, v72, v68, s36
	v_perm_b32 v25, v80, v76, s36
	v_lshl_add_u32 v18, v18, 1, 0
	v_add_u32_e32 v20, v21, v20
	ds_write_b64 v18, v[24:25] offset:55296
	v_perm_b32 v18, v73, v69, s31
	v_perm_b32 v19, v81, v77, s31
	v_lshl_add_u32 v20, v20, 1, 0
	ds_write_b64 v20, v[18:19] offset:55296
	v_add_u32_e32 v18, v28, v21
	v_perm_b32 v22, v73, v69, s36
	v_perm_b32 v23, v81, v77, s36
	v_lshl_add_u32 v18, v18, 1, 0
	ds_write_b64 v18, v[22:23] offset:55296
.LBB0_251:
	s_or_b64 exec, exec, s[0:1]
	s_mul_hi_i32 s0, s33, 0x2aaaaaab
	s_lshr_b32 s1, s0, 31
	s_ashr_i32 s0, s0, 4
	s_add_i32 s25, s0, s1
	s_and_b32 s31, s25, 15
	s_add_i32 s0, s31, 1
	v_cvt_f32_ubyte0_e32 v24, s0
	v_mul_f32_e32 v18, -0.5, v24
	s_mov_b32 s0, 0xc2fc0000
	v_cmp_gt_f32_e32 vcc, s0, v18
	s_and_b64 s[0:1], vcc, exec
	s_cselect_b32 s36, 0xffffffc0, 0
	s_and_b64 s[0:1], s[16:17], exec
	s_cselect_b32 s16, 4, 16
	s_and_b64 s[0:1], s[18:19], exec
	s_cselect_b32 s19, 1, s16
	s_add_i32 s15, s15, s3
	s_lshl_b32 s0, s25, 9
	v_add_u32_e32 v30, s15, v160
	s_and_b32 s0, s0, 0xffffe000
	v_lshlrev_b32_e32 v18, s34, v30
	s_or_b32 s0, s35, s0
	v_add_u32_e32 v158, s0, v18
	v_mov_b64_e32 v[18:19], s[12:13]
	s_movk_i32 s39, 0x4800
	v_mad_i64_i32 v[18:19], s[0:1], v158, s39, v[18:19]
	s_mul_i32 s0, s14, 0xc00
	s_ashr_i32 s1, s0, 31
	s_lshl_b32 s56, s31, 7
	s_add_i32 s18, s33, s2
	s_cmpk_gt_i32 s18, 0xbff
	v_lshl_add_u64 v[18:19], s[0:1], 1, v[18:19]
	s_cselect_b64 s[0:1], -1, 0
	s_cmpk_lt_i32 s18, 0xc00
	s_cselect_b32 s16, s18, s33
	s_ashr_i32 s17, s16, 5
	s_mul_hi_i32 s25, s17, 0x55555556
	s_lshr_b32 s33, s25, 31
	s_add_i32 s25, s25, s33
	s_mul_i32 s25, s25, 3
	s_sub_i32 s17, s17, s25
	s_mul_hi_i32 s25, s16, 0x2aaaaaab
	s_lshr_b32 s33, s25, 31
	s_ashr_i32 s25, s25, 4
	s_add_i32 s25, s25, s33
	s_cmp_eq_u32 s17, 1
	s_cselect_b32 s33, 2, 4
	s_cmp_lg_u32 s17, 0
	s_cselect_b32 s33, s33, 0
	s_lshl_b32 s16, s16, 8
	s_and_b32 s16, s16, 0x1f00
	s_sub_i32 s34, 13, s33
	s_lshr_b32 s37, s16, s34
	s_lshl_b32 s34, s37, s34
	s_sub_i32 s16, s16, s34
	s_add_i32 s38, s16, 0xffffff80
	s_lshl_b32 s16, s25, 9
	s_and_b32 s16, s16, 0xffffe000
	s_mul_hi_i32 s34, s16, 0x4800
	s_mulk_i32 s16, 0x4800
	s_add_u32 s35, s12, s16
	s_mul_i32 s16, s17, 0xc00
	v_lshl_add_u64 v[18:19], v[18:19], 0, s[56:57]
	s_addc_u32 s34, s13, s34
	s_ashr_i32 s17, s16, 31
	v_lshl_add_u64 v[18:19], v[18:19], 0, v[0:1]
	v_mov_b32_e32 v26, v155
	s_lshl_b64 s[16:17], s[16:17], 1
	s_waitcnt vmcnt(0) lgkmcnt(0)
	s_barrier
	s_add_u32 s16, s35, s16
	v_add_u32_e32 v27, 0x200, v26
	s_addc_u32 s17, s34, s17
	s_lshl_b32 s25, s25, 7
	v_ashrrev_i32_e32 v20, 3, v26
	v_ashrrev_i32_e32 v22, 3, v27
	s_and_b32 s25, s25, 0x780
	v_add_u32_e32 v20, s38, v20
	v_add_u32_e32 v22, s38, v22
	s_add_u32 s34, s16, s25
	v_lshlrev_b32_e32 v18, 4, v26
	v_max_i32_e32 v20, 0, v20
	v_max_i32_e32 v22, 0, v22
	s_addc_u32 s35, s17, 0
	v_and_b32_e32 v18, 0x70, v18
	v_mov_b32_e32 v19, v1
	v_lshlrev_b32_e32 v20, s33, v20
	v_lshlrev_b32_e32 v22, s33, v22
	s_add_u32 s16, s34, 0x800
	v_lshl_add_u64 v[18:19], s[34:35], 0, v[18:19]
	v_add_u32_e32 v20, s37, v20
	v_add_u32_e32 v22, s37, v22
	s_addc_u32 s17, s35, 0
	v_mad_u64_u32 v[20:21], s[34:35], v20, s39, v[18:19]
	v_mad_u64_u32 v[22:23], s[34:35], v22, s39, v[18:19]
	global_load_dwordx4 v[106:109], v[20:21], off offset:2048
	global_load_dwordx4 v[98:101], v[22:23], off offset:2048
	v_add_u32_e32 v20, 0x400, v26
	v_add_u32_e32 v22, 0x600, v26
	v_ashrrev_i32_e32 v20, 3, v20
	v_ashrrev_i32_e32 v22, 3, v22
	v_add_u32_e32 v20, s38, v20
	v_add_u32_e32 v22, s38, v22
	v_max_i32_e32 v20, 0, v20
	v_max_i32_e32 v22, 0, v22
	v_lshlrev_b32_e32 v20, s33, v20
	v_lshlrev_b32_e32 v22, s33, v22
	v_add_u32_e32 v20, s37, v20
	v_add_u32_e32 v22, s37, v22
	v_mad_u64_u32 v[20:21], s[34:35], v20, s39, v[18:19]
	v_mad_u64_u32 v[22:23], s[34:35], v22, s39, v[18:19]
	global_load_dwordx4 v[114:117], v[20:21], off offset:2048
	global_load_dwordx4 v[102:105], v[22:23], off offset:2048
	v_add_u32_e32 v20, 0x800, v26
	v_add_u32_e32 v22, 0xa00, v26
	v_ashrrev_i32_e32 v20, 3, v20
	v_ashrrev_i32_e32 v22, 3, v22
	v_add_u32_e32 v20, s38, v20
	v_add_u32_e32 v22, s38, v22
	v_max_i32_e32 v20, 0, v20
	v_max_i32_e32 v22, 0, v22
	v_lshlrev_b32_e32 v20, s33, v20
	v_lshlrev_b32_e32 v22, s33, v22
	v_add_u32_e32 v20, s37, v20
	v_add_u32_e32 v22, s37, v22
	v_mad_u64_u32 v[20:21], s[34:35], v20, s39, v[18:19]
	v_mad_u64_u32 v[18:19], s[34:35], v22, s39, v[18:19]
	s_movk_i32 s25, 0x300
	v_cndmask_b32_e32 v25, 0, v224, vcc
	global_load_dwordx4 v[118:121], v[20:21], off offset:2048
	global_load_dwordx4 v[110:113], v[18:19], off offset:2048
	v_add_u32_e32 v18, 0xfffffe00, v26
	v_cmp_gt_i32_e32 vcc, s25, v26
	s_movk_i32 s25, 0x100
	v_fmac_f32_e32 v25, -0.5, v24
	v_cndmask_b32_e32 v18, v18, v26, vcc
	v_ashrrev_i32_e32 v19, 1, v18
	v_and_b32_e32 v19, -4, v19
	v_add_u32_e32 v19, s38, v19
	v_max_i32_e32 v28, 0, v19
	v_lshlrev_b32_e32 v18, 4, v18
	v_and_b32_e32 v18, 0x70, v18
	v_mov_b32_e32 v19, v1
	v_lshlrev_b32_e32 v20, s33, v28
	v_add_lshl_u32 v22, v28, 1, s33
	v_lshl_add_u64 v[18:19], s[16:17], 0, v[18:19]
	v_add_u32_e32 v20, s37, v20
	v_add_u32_e32 v22, s37, v22
	v_mad_u64_u32 v[20:21], s[34:35], v20, s39, v[18:19]
	v_mad_u64_u32 v[22:23], s[34:35], v22, s39, v[18:19]
	global_load_dwordx4 v[82:85], v[20:21], off offset:2048
	global_load_dwordx4 v[86:89], v[22:23], off offset:2048
	v_add_lshl_u32 v20, v28, 2, s33
	v_add_lshl_u32 v22, v28, 3, s33
	v_add_u32_e32 v20, s37, v20
	v_add_u32_e32 v22, s37, v22
	v_mad_u64_u32 v[20:21], s[34:35], v20, s39, v[18:19]
	v_mad_u64_u32 v[18:19], s[34:35], v22, s39, v[18:19]
	v_cmp_gt_i32_e32 vcc, s25, v26
	global_load_dwordx4 v[90:93], v[20:21], off offset:2048
	global_load_dwordx4 v[94:97], v[18:19], off offset:2048
	v_cndmask_b32_e32 v18, v26, v27, vcc
	v_ashrrev_i32_e32 v19, 1, v18
	v_and_b32_e32 v19, -4, v19
	v_add_u32_e32 v19, s38, v19
	v_max_i32_e32 v26, 0, v19
	v_lshlrev_b32_e32 v18, 4, v18
	v_and_b32_e32 v18, 0x70, v18
	v_mov_b32_e32 v19, v1
	v_lshlrev_b32_e32 v20, s33, v26
	v_lshl_add_u64 v[18:19], s[16:17], 0, v[18:19]
	v_add_u32_e32 v20, s37, v20
	v_add_lshl_u32 v22, v26, 1, s33
	v_mad_u64_u32 v[20:21], s[16:17], v20, s39, v[18:19]
	v_add_u32_e32 v22, s37, v22
	v_mad_u64_u32 v[22:23], s[16:17], v22, s39, v[18:19]
	global_load_dwordx4 v[66:69], v[20:21], off offset:2048
	global_load_dwordx4 v[70:73], v[22:23], off offset:2048
	v_add_lshl_u32 v20, v26, 2, s33
	v_add_u32_e32 v20, s37, v20
	v_add_lshl_u32 v22, v26, 3, s33
	v_mad_u64_u32 v[20:21], s[16:17], v20, s39, v[18:19]
	v_add_u32_e32 v22, s37, v22
	v_mad_u64_u32 v[18:19], s[16:17], v22, s39, v[18:19]
	global_load_dwordx4 v[74:77], v[20:21], off offset:2048
	global_load_dwordx4 v[78:81], v[18:19], off offset:2048
	ds_read_b128 v[18:21], v162
	v_exp_f32_e32 v22, v25
	v_cvt_f32_ubyte0_e32 v23, s19
	s_sub_i32 s16, 0x80, s15
	s_ashr_i32 s16, s16, 5
	v_ldexp_f32 v22, v22, s36
	v_mul_f32_e32 v22, 0x3fb8aa3b, v22
	v_mul_f32_e32 v157, v22, v23
	ds_read_b128 v[22:25], v162 offset:32
	s_waitcnt lgkmcnt(1)
	v_mfma_f32_32x32x16_bf16 v[50:65], v[18:21], v[134:137], 0
	ds_read_b128 v[18:21], v162 offset:64
	ds_read_b128 v[26:29], v162 offset:96
	s_cmpk_lt_i32 s15, 0x80
	s_cselect_b32 s17, s16, 0
	s_cmp_gt_i32 s17, 4
	v_sub_u32_e32 v188, v30, v154
	s_waitcnt lgkmcnt(2)
	v_mfma_f32_32x32x16_bf16 v[50:65], v[22:25], v[130:133], v[50:65]
	s_waitcnt lgkmcnt(1)
	v_mfma_f32_32x32x16_bf16 v[50:65], v[18:21], v[126:129], v[50:65]
	s_waitcnt lgkmcnt(0)
	v_mfma_f32_32x32x16_bf16 v[50:65], v[26:29], v[122:125], v[50:65]
	s_cbranch_scc1 .LBB0_260
	s_cmp_eq_u32 s17, 4
	s_cbranch_scc1 .LBB0_254
	ds_read_b128 v[2:5], v163
	ds_read_b128 v[18:21], v163 offset:32
	s_waitcnt lgkmcnt(1)
	v_mfma_f32_32x32x16_bf16 v[2:17], v[2:5], v[134:137], 0
	s_waitcnt lgkmcnt(0)
	v_mfma_f32_32x32x16_bf16 v[2:17], v[18:21], v[130:133], v[2:17]
	ds_read_b128 v[18:21], v163 offset:64
	s_waitcnt lgkmcnt(0)
	v_mfma_f32_32x32x16_bf16 v[2:17], v[18:21], v[126:129], v[2:17]
	ds_read_b128 v[18:21], v163 offset:96
	s_waitcnt lgkmcnt(0)
	v_mfma_f32_32x32x16_bf16 v[2:17], v[18:21], v[122:125], v[2:17]
